# baseline (speedup 1.0000x reference)
.Lu0_1:
	ds_read_b64_tr_b16 v[178:179], v206 offset:24576
	ds_read_b64_tr_b16 v[180:181], v206 offset:25600
	v_mfma_f32_32x32x16_f16 v[98:113], v[82:85], v[154:157], v[34:49]
	v_add_f32_e32 v86, v66, v67
	v_add_f32_e32 v86, v68, v86
	v_add_f32_e32 v86, v69, v86
	v_add_f32_e32 v86, v70, v86
	v_add_f32_e32 v86, v71, v86
	v_cvt_pk_f16_f32 v158, v66, v67
	v_cvt_pk_f16_f32 v159, v68, v69
	ds_read_b64_tr_b16 v[174:175], v207 offset:24576
	ds_read_b64_tr_b16 v[176:177], v207 offset:25600
	v_add_f32_e32 v66, v72, v86
	v_mfma_f32_32x32x16_f16 v[82:97], v[170:173], v[154:157], v[34:49]
	v_add_f32_e32 v66, v73, v66
	v_add_f32_e32 v66, v74, v66
	v_add_f32_e32 v66, v75, v66
	v_cvt_pk_f16_f32 v160, v70, v71
	v_cvt_pk_f16_f32 v161, v72, v73
	ds_read_b64_tr_b16 v[170:171], v206 offset:26624
	ds_read_b64_tr_b16 v[172:173], v206 offset:27648
	v_mfma_f32_32x32x16_f16 v[98:113], v[166:169], v[146:149], v[98:113]
	v_add_f32_e32 v66, v76, v66
	v_add_f32_e32 v66, v77, v66
	v_add_f32_e32 v66, v78, v66
	v_add_f32_e32 v66, v79, v66
	v_cvt_pk_f16_f32 v150, v74, v75
	v_cvt_pk_f16_f32 v151, v76, v77
	ds_read_b64_tr_b16 v[74:75], v207 offset:26624
	ds_read_b64_tr_b16 v[76:77], v207 offset:27648
	v_mfma_f32_32x32x16_f16 v[82:97], v[162:165], v[146:149], v[82:97]
	v_add_f32_e32 v66, v80, v66
	v_add_f32_e32 v66, v81, v66
	v_add_f32_e32 v66, v50, v66
	v_add_f32_e32 v66, v51, v66
	v_cvt_pk_f16_f32 v152, v78, v79
	v_cvt_pk_f16_f32 v153, v80, v81
	ds_read_b64_tr_b16 v[70:71], v206 offset:28672
	ds_read_b64_tr_b16 v[72:73], v206 offset:29696
	v_mfma_f32_32x32x16_f16 v[98:113], v[126:129], v[138:141], v[98:113]
	v_add_f32_e32 v66, v52, v66
	v_add_f32_e32 v66, v53, v66
	v_add_f32_e32 v66, v54, v66
	v_add_f32_e32 v78, v55, v66
	v_cvt_pk_f16_f32 v142, v50, v51
	v_cvt_pk_f16_f32 v143, v52, v53
	ds_read_b64_tr_b16 v[66:67], v207 offset:28672
	ds_read_b64_tr_b16 v[68:69], v207 offset:29696
	v_mfma_f32_32x32x16_f16 v[82:97], v[122:125], v[138:141], v[82:97]
	v_add_f32_e32 v50, v56, v78
	v_add_f32_e32 v50, v57, v50
	v_add_f32_e32 v50, v58, v50
	v_add_f32_e32 v50, v59, v50
	v_cvt_pk_f16_f32 v144, v54, v55
	v_cvt_pk_f16_f32 v145, v56, v57
	ds_read_b64_tr_b16 v[54:55], v206 offset:30720
	ds_read_b64_tr_b16 v[56:57], v206 offset:31744
	v_mfma_f32_32x32x16_f16 v[98:113], v[118:121], v[134:137], v[98:113]
	v_add_f32_e32 v50, v60, v50
	v_add_f32_e32 v50, v61, v50
	v_add_f32_e32 v50, v62, v50
	v_add_f32_e32 v78, v63, v50
	v_cvt_pk_f16_f32 v130, v58, v59
	v_cvt_pk_f16_f32 v131, v60, v61
	ds_read_b64_tr_b16 v[50:51], v207 offset:30720
	ds_read_b64_tr_b16 v[52:53], v207 offset:31744
	v_mfma_f32_32x32x16_f16 v[82:97], v[114:117], v[134:137], v[82:97]
	v_add_f32_e32 v58, v64, v78
	v_add_f32_e32 v60, v65, v58
	v_cvt_pk_f16_f32 v132, v62, v63
	v_cvt_pk_f16_f32 v133, v64, v65
	v_lshl_add_u64 v[58:59], v[188:189], 0, s[24:25]
	s_add_i32 s26, s42, s36
	s_mov_b32 m0, s26
	s_nop 0
	global_load_lds_dwordx4 v[58:59], off
	v_lshl_add_u64 v[58:59], v[196:197], 0, s[20:21]
	s_add_i32 s26, s39, s35
	s_mov_b32 m0, s26
	s_nop 0
	global_load_lds_dwordx4 v[58:59], off
	v_max_f32_e32 v58, v98, v99
	v_max3_f32 v59, v100, v101, v83
	v_max3_f32 v58, v58, v82, v84
	v_max3_f32 v58, v58, v85, v102
	v_max3_f32 v59, v59, v104, v105
	v_max3_f32 v58, v58, v103, v86
	v_max3_f32 v59, v59, v88, v89
	v_max3_f32 v58, v58, v87, v106
	v_max3_f32 v59, v59, v108, v109
	v_max3_f32 v58, v58, v107, v90
	v_max3_f32 v59, v59, v92, v93
	v_max3_f32 v58, v58, v91, v110
	v_max3_f32 v59, v59, v112, v113
	v_max3_f32 v58, v58, v111, v94
	v_max3_f32 v59, v59, v96, v97
	v_max3_f32 v58, v58, v95, v59
	v_mov_b32_e32 v59, v58
	v_add_f32_e32 v198, v183, v60
	s_nop 0
	v_permlane32_swap_b32_e32 v58, v59
	v_max_f32_e32 v58, v58, v59
	v_cmp_lt_f32_e32 vcc, s41, v58
	s_cmp_lg_u64 vcc, 0
	s_cselect_b64 s[26:27], -1, 0
	s_cbranch_vccnz .Lu0_9

.Lu0_4:
	s_add_i32 s26, s39, 0x2000
	s_cmpk_lg_i32 s39, 0x4000
	s_cselect_b32 s43, s26, 0
	ds_read_b64_tr_b16 v[126:127], v206 offset:32768
	ds_read_b64_tr_b16 v[128:129], v206 offset:33792
	v_mfma_f32_32x32x16_f16 v[66:81], v[58:61], v[154:157], v[34:49]
	v_add_f32_e32 v50, v98, v99
	v_add_f32_e32 v50, v100, v50
	v_add_f32_e32 v50, v101, v50
	v_add_f32_e32 v50, v102, v50
	v_add_f32_e32 v50, v103, v50
	v_cvt_pk_f16_f32 v158, v98, v99
	v_cvt_pk_f16_f32 v159, v100, v101
	ds_read_b64_tr_b16 v[122:123], v207 offset:32768
	ds_read_b64_tr_b16 v[124:125], v207 offset:33792
	v_add_f32_e32 v50, v104, v50
	v_add_f32_e32 v50, v105, v50
	v_add_f32_e32 v50, v106, v50
	v_add_f32_e32 v98, v107, v50
	v_mfma_f32_32x32x16_f16 v[50:65], v[114:117], v[154:157], v[34:49]
	v_cvt_pk_f16_f32 v160, v102, v103
	v_cvt_pk_f16_f32 v161, v104, v105
	ds_read_b64_tr_b16 v[118:119], v206 offset:34816
	ds_read_b64_tr_b16 v[120:121], v206 offset:35840
	v_mfma_f32_32x32x16_f16 v[66:81], v[182:185], v[146:149], v[66:81]
	v_add_f32_e32 v98, v108, v98
	v_add_f32_e32 v98, v109, v98
	v_add_f32_e32 v98, v110, v98
	v_add_f32_e32 v98, v111, v98
	v_cvt_pk_f16_f32 v150, v106, v107
	v_cvt_pk_f16_f32 v151, v108, v109
	ds_read_b64_tr_b16 v[114:115], v207 offset:34816
	ds_read_b64_tr_b16 v[116:117], v207 offset:35840
	v_mfma_f32_32x32x16_f16 v[50:65], v[174:177], v[146:149], v[50:65]
	v_add_f32_e32 v98, v112, v98
	v_add_f32_e32 v98, v113, v98
	v_add_f32_e32 v98, v82, v98
	v_add_f32_e32 v98, v83, v98
	v_cvt_pk_f16_f32 v152, v110, v111
	v_cvt_pk_f16_f32 v153, v112, v113
	ds_read_b64_tr_b16 v[106:107], v206 offset:36864
	ds_read_b64_tr_b16 v[108:109], v206 offset:37888
	v_mfma_f32_32x32x16_f16 v[66:81], v[178:181], v[138:141], v[66:81]
	v_add_f32_e32 v98, v84, v98
	v_add_f32_e32 v98, v85, v98
	v_add_f32_e32 v98, v86, v98
	v_add_f32_e32 v98, v87, v98
	v_cvt_pk_f16_f32 v142, v82, v83
	v_cvt_pk_f16_f32 v143, v84, v85
	ds_read_b64_tr_b16 v[102:103], v207 offset:36864
	ds_read_b64_tr_b16 v[104:105], v207 offset:37888
	v_mfma_f32_32x32x16_f16 v[50:65], v[166:169], v[138:141], v[50:65]
	v_add_f32_e32 v82, v88, v98
	v_add_f32_e32 v82, v89, v82
	v_add_f32_e32 v82, v90, v82
	v_add_f32_e32 v82, v91, v82
	v_cvt_pk_f16_f32 v144, v86, v87
	v_cvt_pk_f16_f32 v145, v88, v89
	ds_read_b64_tr_b16 v[98:99], v206 offset:38912
	ds_read_b64_tr_b16 v[100:101], v206 offset:39936
	v_mfma_f32_32x32x16_f16 v[66:81], v[170:173], v[134:137], v[66:81]
	v_add_f32_e32 v82, v92, v82
	v_add_f32_e32 v82, v93, v82
	v_add_f32_e32 v82, v94, v82
	v_add_f32_e32 v82, v95, v82
	v_cvt_pk_f16_f32 v130, v90, v91
	v_cvt_pk_f16_f32 v131, v92, v93
	ds_read_b64_tr_b16 v[86:87], v207 offset:38912
	ds_read_b64_tr_b16 v[88:89], v207 offset:39936
	v_mfma_f32_32x32x16_f16 v[50:65], v[162:165], v[134:137], v[50:65]
	v_add_f32_e32 v82, v96, v82
	v_add_f32_e32 v84, v97, v82
	v_cvt_pk_f16_f32 v132, v94, v95
	v_cvt_pk_f16_f32 v133, v96, v97
	v_lshl_add_u64 v[82:83], v[188:189], 0, s[2:3]
	s_add_i32 s26, s39, s36
	s_mov_b32 m0, s26
	s_nop 0
	global_load_lds_dwordx4 v[82:83], off
	v_max_f32_e32 v82, v66, v67
	s_nop 1
	v_max3_f32 v83, v68, v69, v51
	v_max3_f32 v82, v82, v50, v52
	v_max3_f32 v82, v82, v53, v70
	v_max3_f32 v83, v83, v72, v73
	v_max3_f32 v82, v82, v71, v54
	v_max3_f32 v83, v83, v56, v57
	v_max3_f32 v82, v82, v55, v74
	v_max3_f32 v83, v83, v76, v77
	v_max3_f32 v82, v82, v75, v58
	v_max3_f32 v83, v83, v60, v61
	v_max3_f32 v82, v82, v59, v78
	v_max3_f32 v83, v83, v80, v81
	v_max3_f32 v82, v82, v79, v62
	v_max3_f32 v83, v83, v64, v65
	v_max3_f32 v82, v82, v63, v83
	v_mov_b32_e32 v83, v82
	v_add_f32_e32 v183, v198, v84
	s_nop 0
	v_permlane32_swap_b32_e32 v82, v83
	v_max_f32_e32 v82, v82, v83
	v_lshl_add_u64 v[196:197], v[196:197], 0, s[22:23]
	s_add_i32 s26, s43, s35
	s_mov_b32 m0, s26
	s_nop 0
	global_load_lds_dwordx4 v[196:197], off
	v_cmp_lt_f32_e32 vcc, s41, v82
	s_cmp_lg_u64 vcc, 0
	s_cselect_b64 s[26:27], -1, 0
	s_cbranch_vccnz .Lu0_12

.Lu1_1:
	ds_read_b64_tr_b16 v[178:179], v206 offset:40960
	ds_read_b64_tr_b16 v[180:181], v206 offset:41984
	v_mfma_f32_32x32x16_f16 v[98:113], v[82:85], v[154:157], v[34:49]
	v_add_f32_e32 v86, v66, v67
	v_add_f32_e32 v86, v68, v86
	v_add_f32_e32 v86, v69, v86
	v_add_f32_e32 v86, v70, v86
	v_add_f32_e32 v86, v71, v86
	v_cvt_pk_f16_f32 v158, v66, v67
	v_cvt_pk_f16_f32 v159, v68, v69
	ds_read_b64_tr_b16 v[174:175], v207 offset:40960
	ds_read_b64_tr_b16 v[176:177], v207 offset:41984
	v_add_f32_e32 v66, v72, v86
	v_mfma_f32_32x32x16_f16 v[82:97], v[170:173], v[154:157], v[34:49]
	v_add_f32_e32 v66, v73, v66
	v_add_f32_e32 v66, v74, v66
	v_add_f32_e32 v66, v75, v66
	v_cvt_pk_f16_f32 v160, v70, v71
	v_cvt_pk_f16_f32 v161, v72, v73
	ds_read_b64_tr_b16 v[170:171], v206 offset:43008
	ds_read_b64_tr_b16 v[172:173], v206 offset:44032
	v_mfma_f32_32x32x16_f16 v[98:113], v[166:169], v[146:149], v[98:113]
	v_add_f32_e32 v66, v76, v66
	v_add_f32_e32 v66, v77, v66
	v_add_f32_e32 v66, v78, v66
	v_add_f32_e32 v66, v79, v66
	v_cvt_pk_f16_f32 v150, v74, v75
	v_cvt_pk_f16_f32 v151, v76, v77
	ds_read_b64_tr_b16 v[74:75], v207 offset:43008
	ds_read_b64_tr_b16 v[76:77], v207 offset:44032
	v_mfma_f32_32x32x16_f16 v[82:97], v[162:165], v[146:149], v[82:97]
	v_add_f32_e32 v66, v80, v66
	v_add_f32_e32 v66, v81, v66
	v_add_f32_e32 v66, v50, v66
	v_add_f32_e32 v66, v51, v66
	v_cvt_pk_f16_f32 v152, v78, v79
	v_cvt_pk_f16_f32 v153, v80, v81
	ds_read_b64_tr_b16 v[70:71], v206 offset:45056
	ds_read_b64_tr_b16 v[72:73], v206 offset:46080
	v_mfma_f32_32x32x16_f16 v[98:113], v[126:129], v[138:141], v[98:113]
	v_add_f32_e32 v66, v52, v66
	v_add_f32_e32 v66, v53, v66
	v_add_f32_e32 v66, v54, v66
	v_add_f32_e32 v78, v55, v66
	v_cvt_pk_f16_f32 v142, v50, v51
	v_cvt_pk_f16_f32 v143, v52, v53
	ds_read_b64_tr_b16 v[66:67], v207 offset:45056
	ds_read_b64_tr_b16 v[68:69], v207 offset:46080
	v_mfma_f32_32x32x16_f16 v[82:97], v[122:125], v[138:141], v[82:97]
	v_add_f32_e32 v50, v56, v78
	v_add_f32_e32 v50, v57, v50
	v_add_f32_e32 v50, v58, v50
	v_add_f32_e32 v50, v59, v50
	v_cvt_pk_f16_f32 v144, v54, v55
	v_cvt_pk_f16_f32 v145, v56, v57
	ds_read_b64_tr_b16 v[54:55], v206 offset:47104
	ds_read_b64_tr_b16 v[56:57], v206 offset:48128
	v_mfma_f32_32x32x16_f16 v[98:113], v[118:121], v[134:137], v[98:113]
	v_add_f32_e32 v50, v60, v50
	v_add_f32_e32 v50, v61, v50
	v_add_f32_e32 v50, v62, v50
	v_add_f32_e32 v78, v63, v50
	v_cvt_pk_f16_f32 v130, v58, v59
	v_cvt_pk_f16_f32 v131, v60, v61
	ds_read_b64_tr_b16 v[50:51], v207 offset:47104
	ds_read_b64_tr_b16 v[52:53], v207 offset:48128
	v_mfma_f32_32x32x16_f16 v[82:97], v[114:117], v[134:137], v[82:97]
	v_add_f32_e32 v58, v64, v78
	v_add_f32_e32 v60, v65, v58
	v_cvt_pk_f16_f32 v132, v62, v63
	v_cvt_pk_f16_f32 v133, v64, v65
	v_lshl_add_u64 v[58:59], v[188:189], 0, s[24:25]
	s_add_i32 s26, s42, s36
	s_mov_b32 m0, s26
	s_nop 0
	global_load_lds_dwordx4 v[58:59], off
	v_lshl_add_u64 v[58:59], v[196:197], 0, s[20:21]
	s_add_i32 s26, s39, s35
	s_mov_b32 m0, s26
	s_nop 0
	global_load_lds_dwordx4 v[58:59], off
	v_max_f32_e32 v58, v98, v99
	v_max3_f32 v59, v100, v101, v83
	v_max3_f32 v58, v58, v82, v84
	v_max3_f32 v58, v58, v85, v102
	v_max3_f32 v59, v59, v104, v105
	v_max3_f32 v58, v58, v103, v86
	v_max3_f32 v59, v59, v88, v89
	v_max3_f32 v58, v58, v87, v106
	v_max3_f32 v59, v59, v108, v109
	v_max3_f32 v58, v58, v107, v90
	v_max3_f32 v59, v59, v92, v93
	v_max3_f32 v58, v58, v91, v110
	v_max3_f32 v59, v59, v112, v113
	v_max3_f32 v58, v58, v111, v94
	v_max3_f32 v59, v59, v96, v97
	v_max3_f32 v58, v58, v95, v59
	v_mov_b32_e32 v59, v58
	v_add_f32_e32 v198, v183, v60
	s_nop 0
	v_permlane32_swap_b32_e32 v58, v59
	v_max_f32_e32 v58, v58, v59
	v_cmp_lt_f32_e32 vcc, s41, v58
	s_cmp_lg_u64 vcc, 0
	s_cselect_b64 s[26:27], -1, 0
	s_cbranch_vccnz .Lu1_9

.Lu1_4:
	s_add_i32 s26, s39, 0x2000
	s_cmpk_lg_i32 s39, 0x4000
	s_cselect_b32 s43, s26, 0
	ds_read_b64_tr_b16 v[126:127], v206 offset:24576
	ds_read_b64_tr_b16 v[128:129], v206 offset:25600
	v_mfma_f32_32x32x16_f16 v[66:81], v[58:61], v[154:157], v[34:49]
	v_add_f32_e32 v50, v98, v99
	v_add_f32_e32 v50, v100, v50
	v_add_f32_e32 v50, v101, v50
	v_add_f32_e32 v50, v102, v50
	v_add_f32_e32 v50, v103, v50
	v_cvt_pk_f16_f32 v158, v98, v99
	v_cvt_pk_f16_f32 v159, v100, v101
	ds_read_b64_tr_b16 v[122:123], v207 offset:24576
	ds_read_b64_tr_b16 v[124:125], v207 offset:25600
	v_add_f32_e32 v50, v104, v50
	v_add_f32_e32 v50, v105, v50
	v_add_f32_e32 v50, v106, v50
	v_add_f32_e32 v98, v107, v50
	v_mfma_f32_32x32x16_f16 v[50:65], v[114:117], v[154:157], v[34:49]
	v_cvt_pk_f16_f32 v160, v102, v103
	v_cvt_pk_f16_f32 v161, v104, v105
	ds_read_b64_tr_b16 v[118:119], v206 offset:26624
	ds_read_b64_tr_b16 v[120:121], v206 offset:27648
	v_mfma_f32_32x32x16_f16 v[66:81], v[182:185], v[146:149], v[66:81]
	v_add_f32_e32 v98, v108, v98
	v_add_f32_e32 v98, v109, v98
	v_add_f32_e32 v98, v110, v98
	v_add_f32_e32 v98, v111, v98
	v_cvt_pk_f16_f32 v150, v106, v107
	v_cvt_pk_f16_f32 v151, v108, v109
	ds_read_b64_tr_b16 v[114:115], v207 offset:26624
	ds_read_b64_tr_b16 v[116:117], v207 offset:27648
	v_mfma_f32_32x32x16_f16 v[50:65], v[174:177], v[146:149], v[50:65]
	v_add_f32_e32 v98, v112, v98
	v_add_f32_e32 v98, v113, v98
	v_add_f32_e32 v98, v82, v98
	v_add_f32_e32 v98, v83, v98
	v_cvt_pk_f16_f32 v152, v110, v111
	v_cvt_pk_f16_f32 v153, v112, v113
	ds_read_b64_tr_b16 v[106:107], v206 offset:28672
	ds_read_b64_tr_b16 v[108:109], v206 offset:29696
	v_mfma_f32_32x32x16_f16 v[66:81], v[178:181], v[138:141], v[66:81]
	v_add_f32_e32 v98, v84, v98
	v_add_f32_e32 v98, v85, v98
	v_add_f32_e32 v98, v86, v98
	v_add_f32_e32 v98, v87, v98
	v_cvt_pk_f16_f32 v142, v82, v83
	v_cvt_pk_f16_f32 v143, v84, v85
	ds_read_b64_tr_b16 v[102:103], v207 offset:28672
	ds_read_b64_tr_b16 v[104:105], v207 offset:29696
	v_mfma_f32_32x32x16_f16 v[50:65], v[166:169], v[138:141], v[50:65]
	v_add_f32_e32 v82, v88, v98
	v_add_f32_e32 v82, v89, v82
	v_add_f32_e32 v82, v90, v82
	v_add_f32_e32 v82, v91, v82
	v_cvt_pk_f16_f32 v144, v86, v87
	v_cvt_pk_f16_f32 v145, v88, v89
	ds_read_b64_tr_b16 v[98:99], v206 offset:30720
	ds_read_b64_tr_b16 v[100:101], v206 offset:31744
	v_mfma_f32_32x32x16_f16 v[66:81], v[170:173], v[134:137], v[66:81]
	v_add_f32_e32 v82, v92, v82
	v_add_f32_e32 v82, v93, v82
	v_add_f32_e32 v82, v94, v82
	v_add_f32_e32 v82, v95, v82
	v_cvt_pk_f16_f32 v130, v90, v91
	v_cvt_pk_f16_f32 v131, v92, v93
	ds_read_b64_tr_b16 v[86:87], v207 offset:30720
	ds_read_b64_tr_b16 v[88:89], v207 offset:31744
	v_mfma_f32_32x32x16_f16 v[50:65], v[162:165], v[134:137], v[50:65]
	v_add_f32_e32 v82, v96, v82
	v_add_f32_e32 v84, v97, v82
	v_cvt_pk_f16_f32 v132, v94, v95
	v_cvt_pk_f16_f32 v133, v96, v97
	v_lshl_add_u64 v[82:83], v[188:189], 0, s[2:3]
	s_add_i32 s26, s39, s36
	s_mov_b32 m0, s26
	s_nop 0
	global_load_lds_dwordx4 v[82:83], off
	v_max_f32_e32 v82, v66, v67
	s_nop 1
	v_max3_f32 v83, v68, v69, v51
	v_max3_f32 v82, v82, v50, v52
	v_max3_f32 v82, v82, v53, v70
	v_max3_f32 v83, v83, v72, v73
	v_max3_f32 v82, v82, v71, v54
	v_max3_f32 v83, v83, v56, v57
	v_max3_f32 v82, v82, v55, v74
	v_max3_f32 v83, v83, v76, v77
	v_max3_f32 v82, v82, v75, v58
	v_max3_f32 v83, v83, v60, v61
	v_max3_f32 v82, v82, v59, v78
	v_max3_f32 v83, v83, v80, v81
	v_max3_f32 v82, v82, v79, v62
	v_max3_f32 v83, v83, v64, v65
	v_max3_f32 v82, v82, v63, v83
	v_mov_b32_e32 v83, v82
	v_add_f32_e32 v183, v198, v84
	s_nop 0
	v_permlane32_swap_b32_e32 v82, v83
	v_max_f32_e32 v82, v82, v83
	v_lshl_add_u64 v[196:197], v[196:197], 0, s[22:23]
	s_add_i32 s26, s43, s35
	s_mov_b32 m0, s26
	s_nop 0
	global_load_lds_dwordx4 v[196:197], off
	v_cmp_lt_f32_e32 vcc, s41, v82
	s_cmp_lg_u64 vcc, 0
	s_cselect_b64 s[26:27], -1, 0
	s_cbranch_vccnz .Lu1_12

.Lu2_1:
	ds_read_b64_tr_b16 v[178:179], v206 offset:32768
	ds_read_b64_tr_b16 v[180:181], v206 offset:33792
	v_mfma_f32_32x32x16_f16 v[98:113], v[82:85], v[154:157], v[34:49]
	v_add_f32_e32 v86, v66, v67
	v_add_f32_e32 v86, v68, v86
	v_add_f32_e32 v86, v69, v86
	v_add_f32_e32 v86, v70, v86
	v_add_f32_e32 v86, v71, v86
	v_cvt_pk_f16_f32 v158, v66, v67
	v_cvt_pk_f16_f32 v159, v68, v69
	ds_read_b64_tr_b16 v[174:175], v207 offset:32768
	ds_read_b64_tr_b16 v[176:177], v207 offset:33792
	v_add_f32_e32 v66, v72, v86
	v_mfma_f32_32x32x16_f16 v[82:97], v[170:173], v[154:157], v[34:49]
	v_add_f32_e32 v66, v73, v66
	v_add_f32_e32 v66, v74, v66
	v_add_f32_e32 v66, v75, v66
	v_cvt_pk_f16_f32 v160, v70, v71
	v_cvt_pk_f16_f32 v161, v72, v73
	ds_read_b64_tr_b16 v[170:171], v206 offset:34816
	ds_read_b64_tr_b16 v[172:173], v206 offset:35840
	v_mfma_f32_32x32x16_f16 v[98:113], v[166:169], v[146:149], v[98:113]
	v_add_f32_e32 v66, v76, v66
	v_add_f32_e32 v66, v77, v66
	v_add_f32_e32 v66, v78, v66
	v_add_f32_e32 v66, v79, v66
	v_cvt_pk_f16_f32 v150, v74, v75
	v_cvt_pk_f16_f32 v151, v76, v77
	ds_read_b64_tr_b16 v[74:75], v207 offset:34816
	ds_read_b64_tr_b16 v[76:77], v207 offset:35840
	v_mfma_f32_32x32x16_f16 v[82:97], v[162:165], v[146:149], v[82:97]
	v_add_f32_e32 v66, v80, v66
	v_add_f32_e32 v66, v81, v66
	v_add_f32_e32 v66, v50, v66
	v_add_f32_e32 v66, v51, v66
	v_cvt_pk_f16_f32 v152, v78, v79
	v_cvt_pk_f16_f32 v153, v80, v81
	ds_read_b64_tr_b16 v[70:71], v206 offset:36864
	ds_read_b64_tr_b16 v[72:73], v206 offset:37888
	v_mfma_f32_32x32x16_f16 v[98:113], v[126:129], v[138:141], v[98:113]
	v_add_f32_e32 v66, v52, v66
	v_add_f32_e32 v66, v53, v66
	v_add_f32_e32 v66, v54, v66
	v_add_f32_e32 v78, v55, v66
	v_cvt_pk_f16_f32 v142, v50, v51
	v_cvt_pk_f16_f32 v143, v52, v53
	ds_read_b64_tr_b16 v[66:67], v207 offset:36864
	ds_read_b64_tr_b16 v[68:69], v207 offset:37888
	v_mfma_f32_32x32x16_f16 v[82:97], v[122:125], v[138:141], v[82:97]
	v_add_f32_e32 v50, v56, v78
	v_add_f32_e32 v50, v57, v50
	v_add_f32_e32 v50, v58, v50
	v_add_f32_e32 v50, v59, v50
	v_cvt_pk_f16_f32 v144, v54, v55
	v_cvt_pk_f16_f32 v145, v56, v57
	ds_read_b64_tr_b16 v[54:55], v206 offset:38912
	ds_read_b64_tr_b16 v[56:57], v206 offset:39936
	v_mfma_f32_32x32x16_f16 v[98:113], v[118:121], v[134:137], v[98:113]
	v_add_f32_e32 v50, v60, v50
	v_add_f32_e32 v50, v61, v50
	v_add_f32_e32 v50, v62, v50
	v_add_f32_e32 v78, v63, v50
	v_cvt_pk_f16_f32 v130, v58, v59
	v_cvt_pk_f16_f32 v131, v60, v61
	ds_read_b64_tr_b16 v[50:51], v207 offset:38912
	ds_read_b64_tr_b16 v[52:53], v207 offset:39936
	v_mfma_f32_32x32x16_f16 v[82:97], v[114:117], v[134:137], v[82:97]
	v_add_f32_e32 v58, v64, v78
	v_add_f32_e32 v60, v65, v58
	v_cvt_pk_f16_f32 v132, v62, v63
	v_cvt_pk_f16_f32 v133, v64, v65
	v_lshl_add_u64 v[58:59], v[188:189], 0, s[24:25]
	s_add_i32 s26, s42, s36
	s_mov_b32 m0, s26
	s_nop 0
	global_load_lds_dwordx4 v[58:59], off
	v_lshl_add_u64 v[58:59], v[196:197], 0, s[20:21]
	s_add_i32 s26, s39, s35
	s_mov_b32 m0, s26
	s_nop 0
	global_load_lds_dwordx4 v[58:59], off
	v_max_f32_e32 v58, v98, v99
	v_max3_f32 v59, v100, v101, v83
	v_max3_f32 v58, v58, v82, v84
	v_max3_f32 v58, v58, v85, v102
	v_max3_f32 v59, v59, v104, v105
	v_max3_f32 v58, v58, v103, v86
	v_max3_f32 v59, v59, v88, v89
	v_max3_f32 v58, v58, v87, v106
	v_max3_f32 v59, v59, v108, v109
	v_max3_f32 v58, v58, v107, v90
	v_max3_f32 v59, v59, v92, v93
	v_max3_f32 v58, v58, v91, v110
	v_max3_f32 v59, v59, v112, v113
	v_max3_f32 v58, v58, v111, v94
	v_max3_f32 v59, v59, v96, v97
	v_max3_f32 v58, v58, v95, v59
	v_mov_b32_e32 v59, v58
	v_add_f32_e32 v198, v183, v60
	s_nop 0
	v_permlane32_swap_b32_e32 v58, v59
	v_max_f32_e32 v58, v58, v59
	v_cmp_lt_f32_e32 vcc, s41, v58
	s_cmp_lg_u64 vcc, 0
	s_cselect_b64 s[26:27], -1, 0
	s_cbranch_vccnz .Lu2_9

.Lu2_4:
	s_add_i32 s26, s39, 0x2000
	s_cmpk_lg_i32 s39, 0x4000
	s_cselect_b32 s43, s26, 0
	ds_read_b64_tr_b16 v[126:127], v206 offset:40960
	ds_read_b64_tr_b16 v[128:129], v206 offset:41984
	v_mfma_f32_32x32x16_f16 v[66:81], v[58:61], v[154:157], v[34:49]
	v_add_f32_e32 v50, v98, v99
	v_add_f32_e32 v50, v100, v50
	v_add_f32_e32 v50, v101, v50
	v_add_f32_e32 v50, v102, v50
	v_add_f32_e32 v50, v103, v50
	v_cvt_pk_f16_f32 v158, v98, v99
	v_cvt_pk_f16_f32 v159, v100, v101
	ds_read_b64_tr_b16 v[122:123], v207 offset:40960
	ds_read_b64_tr_b16 v[124:125], v207 offset:41984
	v_add_f32_e32 v50, v104, v50
	v_add_f32_e32 v50, v105, v50
	v_add_f32_e32 v50, v106, v50
	v_add_f32_e32 v98, v107, v50
	v_mfma_f32_32x32x16_f16 v[50:65], v[114:117], v[154:157], v[34:49]
	v_cvt_pk_f16_f32 v160, v102, v103
	v_cvt_pk_f16_f32 v161, v104, v105
	ds_read_b64_tr_b16 v[118:119], v206 offset:43008
	ds_read_b64_tr_b16 v[120:121], v206 offset:44032
	v_mfma_f32_32x32x16_f16 v[66:81], v[182:185], v[146:149], v[66:81]
	v_add_f32_e32 v98, v108, v98
	v_add_f32_e32 v98, v109, v98
	v_add_f32_e32 v98, v110, v98
	v_add_f32_e32 v98, v111, v98
	v_cvt_pk_f16_f32 v150, v106, v107
	v_cvt_pk_f16_f32 v151, v108, v109
	ds_read_b64_tr_b16 v[114:115], v207 offset:43008
	ds_read_b64_tr_b16 v[116:117], v207 offset:44032
	v_mfma_f32_32x32x16_f16 v[50:65], v[174:177], v[146:149], v[50:65]
	v_add_f32_e32 v98, v112, v98
	v_add_f32_e32 v98, v113, v98
	v_add_f32_e32 v98, v82, v98
	v_add_f32_e32 v98, v83, v98
	v_cvt_pk_f16_f32 v152, v110, v111
	v_cvt_pk_f16_f32 v153, v112, v113
	ds_read_b64_tr_b16 v[106:107], v206 offset:45056
	ds_read_b64_tr_b16 v[108:109], v206 offset:46080
	v_mfma_f32_32x32x16_f16 v[66:81], v[178:181], v[138:141], v[66:81]
	v_add_f32_e32 v98, v84, v98
	v_add_f32_e32 v98, v85, v98
	v_add_f32_e32 v98, v86, v98
	v_add_f32_e32 v98, v87, v98
	v_cvt_pk_f16_f32 v142, v82, v83
	v_cvt_pk_f16_f32 v143, v84, v85
	ds_read_b64_tr_b16 v[102:103], v207 offset:45056
	ds_read_b64_tr_b16 v[104:105], v207 offset:46080
	v_mfma_f32_32x32x16_f16 v[50:65], v[166:169], v[138:141], v[50:65]
	v_add_f32_e32 v82, v88, v98
	v_add_f32_e32 v82, v89, v82
	v_add_f32_e32 v82, v90, v82
	v_add_f32_e32 v82, v91, v82
	v_cvt_pk_f16_f32 v144, v86, v87
	v_cvt_pk_f16_f32 v145, v88, v89
	ds_read_b64_tr_b16 v[98:99], v206 offset:47104
	ds_read_b64_tr_b16 v[100:101], v206 offset:48128
	v_mfma_f32_32x32x16_f16 v[66:81], v[170:173], v[134:137], v[66:81]
	v_add_f32_e32 v82, v92, v82
	v_add_f32_e32 v82, v93, v82
	v_add_f32_e32 v82, v94, v82
	v_add_f32_e32 v82, v95, v82
	v_cvt_pk_f16_f32 v130, v90, v91
	v_cvt_pk_f16_f32 v131, v92, v93
	ds_read_b64_tr_b16 v[86:87], v207 offset:47104
	ds_read_b64_tr_b16 v[88:89], v207 offset:48128
	v_mfma_f32_32x32x16_f16 v[50:65], v[162:165], v[134:137], v[50:65]
	v_add_f32_e32 v82, v96, v82
	v_add_f32_e32 v84, v97, v82
	v_cvt_pk_f16_f32 v132, v94, v95
	v_cvt_pk_f16_f32 v133, v96, v97
	v_lshl_add_u64 v[82:83], v[188:189], 0, s[2:3]
	s_add_i32 s26, s39, s36
	s_mov_b32 m0, s26
	s_nop 0
	global_load_lds_dwordx4 v[82:83], off
	v_max_f32_e32 v82, v66, v67
	s_nop 1
	v_max3_f32 v83, v68, v69, v51
	v_max3_f32 v82, v82, v50, v52
	v_max3_f32 v82, v82, v53, v70
	v_max3_f32 v83, v83, v72, v73
	v_max3_f32 v82, v82, v71, v54
	v_max3_f32 v83, v83, v56, v57
	v_max3_f32 v82, v82, v55, v74
	v_max3_f32 v83, v83, v76, v77
	v_max3_f32 v82, v82, v75, v58
	v_max3_f32 v83, v83, v60, v61
	v_max3_f32 v82, v82, v59, v78
	v_max3_f32 v83, v83, v80, v81
	v_max3_f32 v82, v82, v79, v62
	v_max3_f32 v83, v83, v64, v65
	v_max3_f32 v82, v82, v63, v83
	v_mov_b32_e32 v83, v82
	v_add_f32_e32 v183, v198, v84
	s_nop 0
	v_permlane32_swap_b32_e32 v82, v83
	v_max_f32_e32 v82, v82, v83
	v_lshl_add_u64 v[196:197], v[196:197], 0, s[22:23]
	s_add_i32 s26, s43, s35
	s_mov_b32 m0, s26
	s_nop 0
	global_load_lds_dwordx4 v[196:197], off
	v_cmp_lt_f32_e32 vcc, s41, v82
	s_cmp_lg_u64 vcc, 0
	s_cselect_b64 s[26:27], -1, 0
	s_cbranch_vccnz .Lu2_12
